# v65 + non-temporal hint on prep_moe's converted expert-weight stores (written beside in-proj, read ~5 phases later)
# speedup vs baseline: 1.0145x; 1.0145x over previous
; #define LAS __attribute__((address_space(3)))
; __device__ __forceinline__ unsigned pk2(float lo, float hi) { f32x2_cv_ v = {lo, hi}; return __builtin_bit_cast(unsigned, __builtin_convertvector(v, bf16x2_cv_)); }
; __device__ __forceinline__ void prep_item64(const float* W, int ldw, int srccol0, const float* g, bf16_t* dstrow0, int K, int k0, LAS float* scr, int lane) {
;     ...
;     for (int i = 0; i < 16; ++i) { const float gg = g ? g[k0 + 4 * i + kq] : 1.f; LAS float* d = scr + (4 * i + kq) * 65 + n4; d[0] = v[i][0] * gg; d[1] = v[i][1] * gg; d[2] = v[i][2] * gg; d[3] = v[i][3] * gg; }
;     asm volatile("s_waitcnt lgkmcnt(0)" ::: "memory");
;     const int c = lane & 7;
; #pragma unroll
;     for (int j = 0; j < 8; ++j) { const int n = (lane >> 3) + 8 * j; const LAS float* s = scr + (8 * c) * 65 + n;
;         u32x4 o; o.x = pk2(s[0 * 65], s[1 * 65]); o.y = pk2(s[2 * 65], s[3 * 65]); o.z = pk2(s[4 * 65], s[5 * 65]); o.w = pk2(s[6 * 65], s[7 * 65]);
;         *(u32x4*)(dstrow0 + (size_t)n * K + k0 + 8 * c) = o; }
;     asm volatile("s_waitcnt lgkmcnt(0)" ::: "memory");
; __device__ __forceinline__ void phase_prep_moe(Frame& F, int l, int part) {
;     ...
;         if (r < I_G1) { const int kb = r >> 3, n0 = (r & 7) * 64; const int pn = n0 >> 8, c = n0 & 255;
;             const float* W = (c < 128 ? P.in[17] : P.in[18]) + ((size_t)l * NEXP + e) * DM * DEXP; const int src = pn * 128 + (c & 127);
;             prep_item64(W, DEXP, src, P.in[12] + l * DM, WG1 + ((size_t)e * 512 + n0) * DM, DM, kb * 64, scr, F.lane); }
.LBB0_294:
	s_add_u32 s8, s2, s16
	s_waitcnt vmcnt(0)
	v_pk_mul_f32 v[2:3], v[2:3], v[0:1] op_sel_hi:[1,0]
	s_addc_u32 s9, s3, s17
	s_lshl_b32 s15, s29, 17
	ds_write2_b32 v112, v2, v3 offset1:1
	v_pk_mul_f32 v[2:3], v[4:5], v[0:1] op_sel_hi:[1,0]
	s_and_b32 s15, s15, 0xe0000
	ds_write2_b32 v111, v2, v3 offset1:1
	s_add_u32 s16, s8, s15
	s_waitcnt lgkmcnt(0)
	s_addc_u32 s17, s9, 0
	s_ashr_i32 s15, s14, 31
	ds_read_b32 v0, v107
	ds_read_b32 v2, v107 offset:260
	ds_read_b32 v3, v107 offset:520
	ds_read_b32 v4, v107 offset:780
	ds_read_b32 v5, v107 offset:1040
	ds_read_b32 v8, v107 offset:1300
	ds_read_b32 v9, v107 offset:1560
	ds_read_b32 v10, v107 offset:1820
	s_lshl_b64 s[8:9], s[14:15], 1
	s_add_u32 s8, s16, s8
	s_addc_u32 s9, s17, s9
	v_mov_b32_e32 v103, v1
	v_lshl_add_u64 v[6:7], s[8:9], 0, v[102:103]
	s_waitcnt lgkmcnt(6)
	v_cvt_pk_bf16_f32 v2, v0, v2
	s_waitcnt lgkmcnt(4)
	v_cvt_pk_bf16_f32 v3, v3, v4
	s_waitcnt lgkmcnt(2)
	v_cvt_pk_bf16_f32 v4, v5, v8
	s_waitcnt lgkmcnt(0)
	v_cvt_pk_bf16_f32 v5, v9, v10
	v_lshl_add_u64 v[8:9], v[6:7], 0, v[86:87]
	flat_store_dwordx4 v[8:9], v[2:5] nt
	ds_read_b32 v0, v107 offset:32
	ds_read_b32 v2, v107 offset:292
	ds_read_b32 v3, v107 offset:552
	ds_read_b32 v4, v107 offset:812
	ds_read_b32 v5, v107 offset:1072
	ds_read_b32 v8, v107 offset:1332
	ds_read_b32 v9, v107 offset:1592
	ds_read_b32 v10, v107 offset:1852
	s_waitcnt lgkmcnt(0)
	v_cvt_pk_bf16_f32 v2, v0, v2
	v_cvt_pk_bf16_f32 v3, v3, v4
	v_cvt_pk_bf16_f32 v4, v5, v8
	v_cvt_pk_bf16_f32 v5, v9, v10
	v_lshl_add_u64 v[8:9], v[6:7], 0, v[88:89]
	flat_store_dwordx4 v[8:9], v[2:5] nt
	ds_read_b32 v0, v107 offset:64
	ds_read_b32 v2, v107 offset:324
	ds_read_b32 v3, v107 offset:584
	ds_read_b32 v4, v107 offset:844
	ds_read_b32 v5, v107 offset:1104
	ds_read_b32 v8, v107 offset:1364
	ds_read_b32 v9, v107 offset:1624
	ds_read_b32 v10, v107 offset:1884
	s_waitcnt lgkmcnt(0)
	v_cvt_pk_bf16_f32 v2, v0, v2
	v_cvt_pk_bf16_f32 v3, v3, v4
	v_cvt_pk_bf16_f32 v4, v5, v8
	v_cvt_pk_bf16_f32 v5, v9, v10
	v_lshl_add_u64 v[8:9], v[6:7], 0, v[90:91]
	flat_store_dwordx4 v[8:9], v[2:5] nt
	ds_read_b32 v0, v107 offset:96
	ds_read_b32 v2, v107 offset:356
	ds_read_b32 v3, v107 offset:616
	ds_read_b32 v4, v107 offset:876
	ds_read_b32 v5, v107 offset:1136
	ds_read_b32 v8, v107 offset:1396
	ds_read_b32 v9, v107 offset:1656
	ds_read_b32 v10, v107 offset:1916
	s_waitcnt lgkmcnt(0)
	v_cvt_pk_bf16_f32 v2, v0, v2
	v_cvt_pk_bf16_f32 v3, v3, v4
	v_cvt_pk_bf16_f32 v4, v5, v8
	v_cvt_pk_bf16_f32 v5, v9, v10
	v_lshl_add_u64 v[8:9], v[6:7], 0, v[92:93]
	flat_store_dwordx4 v[8:9], v[2:5] nt
	ds_read_b32 v0, v107 offset:128
	ds_read_b32 v2, v107 offset:388
	ds_read_b32 v3, v107 offset:648
	ds_read_b32 v4, v107 offset:908
	ds_read_b32 v5, v107 offset:1168
	ds_read_b32 v8, v107 offset:1428
	ds_read_b32 v9, v107 offset:1688
	ds_read_b32 v10, v107 offset:1948
	s_waitcnt lgkmcnt(0)
	v_cvt_pk_bf16_f32 v2, v0, v2
	v_cvt_pk_bf16_f32 v3, v3, v4
	v_cvt_pk_bf16_f32 v4, v5, v8
	v_cvt_pk_bf16_f32 v5, v9, v10
	v_lshl_add_u64 v[8:9], v[6:7], 0, v[94:95]
	flat_store_dwordx4 v[8:9], v[2:5] nt
	ds_read_b32 v0, v107 offset:160
	ds_read_b32 v2, v107 offset:420
	ds_read_b32 v3, v107 offset:680
	ds_read_b32 v4, v107 offset:940
	ds_read_b32 v5, v107 offset:1200
	ds_read_b32 v8, v107 offset:1460
	ds_read_b32 v9, v107 offset:1720
	ds_read_b32 v10, v107 offset:1980
	s_waitcnt lgkmcnt(0)
	v_cvt_pk_bf16_f32 v2, v0, v2
	v_cvt_pk_bf16_f32 v3, v3, v4
	v_cvt_pk_bf16_f32 v4, v5, v8
	v_cvt_pk_bf16_f32 v5, v9, v10
	v_lshl_add_u64 v[8:9], v[6:7], 0, v[96:97]
	flat_store_dwordx4 v[8:9], v[2:5] nt
	ds_read_b32 v0, v107 offset:192
	ds_read_b32 v2, v107 offset:452
	ds_read_b32 v3, v107 offset:712
	ds_read_b32 v4, v107 offset:972
	ds_read_b32 v5, v107 offset:1232
	ds_read_b32 v8, v107 offset:1492
	ds_read_b32 v9, v107 offset:1752
	ds_read_b32 v10, v107 offset:2012
	s_waitcnt lgkmcnt(0)
	v_cvt_pk_bf16_f32 v2, v0, v2
	v_cvt_pk_bf16_f32 v3, v3, v4
	v_cvt_pk_bf16_f32 v4, v5, v8
	v_cvt_pk_bf16_f32 v5, v9, v10
	v_lshl_add_u64 v[8:9], v[6:7], 0, v[98:99]
	flat_store_dwordx4 v[8:9], v[2:5] nt
	ds_read_b32 v0, v107 offset:224
	ds_read_b32 v2, v107 offset:484
	ds_read_b32 v3, v107 offset:744
	ds_read_b32 v4, v107 offset:1004
	ds_read_b32 v5, v107 offset:1264
	ds_read_b32 v8, v107 offset:1524
	ds_read_b32 v9, v107 offset:1784
	ds_read_b32 v10, v107 offset:2044
	s_waitcnt lgkmcnt(0)
	v_cvt_pk_bf16_f32 v2, v0, v2
	v_cvt_pk_bf16_f32 v3, v3, v4
	v_cvt_pk_bf16_f32 v4, v5, v8
	v_lshl_add_u64 v[6:7], v[6:7], 0, v[100:101]
	v_cvt_pk_bf16_f32 v5, v9, v10
	flat_store_dwordx4 v[6:7], v[2:5] nt
	s_waitcnt lgkmcnt(0)

; #define LAS __attribute__((address_space(3)))
; __device__ __forceinline__ void prep_item64(const float* W, int ldw, int srccol0, const float* g, bf16_t* dstrow0, int K, int k0, LAS float* scr, int lane) {
;     f32x4 v[16];
;     const int kq = lane >> 4, n4 = (lane & 15) * 4;
; #pragma unroll
;     for (int i = 0; i < 16; ++i) v[i] = __builtin_nontemporal_load((const f32x4*)(W + (size_t)(k0 + 4 * i + kq) * ldw + srccol0 + n4));
; __device__ __forceinline__ void phase_prep_moe(Frame& F, int l, int part) {
;     ...
;     for (int rnd = 0; rnd * slots < NEXP * I_E; ++rnd)
;       for (int k = k0; k < k1; ++k) {
;         const int it = rnd * slots + base + k; if (it >= NEXP * I_E) break;
;         const int e = it / I_E; int r = it % I_E;
;         if (r < I_G1) { const int kb = r >> 3, n0 = (r & 7) * 64; const int pn = n0 >> 8, c = n0 & 255;
;             const float* W = (c < 128 ? P.in[17] : P.in[18]) + ((size_t)l * NEXP + e) * DM * DEXP; const int src = pn * 128 + (c & 127);
;             prep_item64(W, DEXP, src, P.in[12] + l * DM, WG1 + ((size_t)e * 512 + n0) * DM, DM, kb * 64, scr, F.lane); }
;         else { r -= I_G1; const int kb = r >> 4, n0 = (r & 15) * 64;
;             prep_item64(P.in[19] + ((size_t)l * NEXP + e) * DEXP * DM, DM, n0, nullptr, WD + ((size_t)e * DM + n0) * DEXP, DEXP, kb * 64, scr, F.lane); }
.LBB0_297:
	s_cmpk_gt_i32 s27, 0x17ff
	s_mov_b64 s[8:9], -1
	s_cbranch_scc1 .LBB0_296
	s_mul_hi_i32 s8, s27, 0x2aaaaaab
	s_lshr_b32 s9, s8, 31
	s_ashr_i32 s8, s8, 5
	s_add_i32 s8, s8, s9
	s_mul_i32 s9, s8, 0xc0
	s_sub_i32 s29, s27, s9
	s_lshl_b32 s18, s29, 6
	s_cmpk_gt_i32 s29, 0x7f
	s_mov_b64 s[14:15], -1
	v_add_u32_e32 v137, 0x828, v106
	v_add_u32_e32 v136, 0xc30, v106
	v_add_u32_e32 v135, 0xc38, v106
	v_add_u32_e32 v133, 0x1040, v106
	v_add_u32_e32 v134, 0x1048, v106
	v_add_u32_e32 v132, 0x1450, v106
	v_add_u32_e32 v131, 0x1458, v106
	v_add_u32_e32 v129, 0x1860, v106
	v_add_u32_e32 v130, 0x1868, v106
	v_add_u32_e32 v128, 0x1c70, v106
	v_add_u32_e32 v127, 0x1c78, v106
	v_add_u32_e32 v125, 0x2080, v106
	v_add_u32_e32 v126, 0x2088, v106
	v_add_u32_e32 v124, 0x2490, v106
	v_add_u32_e32 v123, 0x2498, v106
	v_add_u32_e32 v121, 0x28a0, v106
	v_add_u32_e32 v122, 0x28a8, v106
	v_add_u32_e32 v120, 0x2cb0, v106
	v_add_u32_e32 v119, 0x2cb8, v106
	v_add_u32_e32 v117, 0x30c0, v106
	v_add_u32_e32 v118, 0x30c8, v106
	v_add_u32_e32 v116, 0x34d0, v106
	v_add_u32_e32 v115, 0x34d8, v106
	v_add_u32_e32 v113, 0x38e0, v106
	v_add_u32_e32 v114, 0x38e8, v106
	v_add_u32_e32 v112, 0x3cf0, v106
	v_add_u32_e32 v111, 0x3cf8, v106
	v_lshlrev_b32_e32 v0, 2, v66
	v_lshlrev_b32_e32 v102, 1, v68
	s_cbranch_scc0 .LBB0_300
	s_ashr_i32 s9, s8, 31
	s_and_b32 s16, s18, 0x3c0
	s_lshl_b64 s[14:15], s[8:9], 20
	s_add_u32 s17, s66, s14
	s_addc_u32 s19, s67, s15
	s_lshl_b64 s[14:15], s[8:9], 19
	s_add_u32 s9, s6, s14
	s_addc_u32 s14, s7, s15
	s_lshl_b32 s15, s16, 9
	s_add_u32 s9, s9, s15
	s_addc_u32 s30, s14, 0
	s_lshl_b32 s14, s29, 2
	s_and_b32 s14, s14, 0x7fffffc0
	s_add_i32 s88, s14, 0xfffffe00
	s_lshl_b32 s14, s16, 2
	v_or_b32_e32 v62, s88, v69
	s_add_u32 s14, s17, s14
	s_addc_u32 s15, s19, 0
	v_mov_b32_e32 v63, v1
	v_or_b32_e32 v4, 4, v62
	v_mov_b32_e32 v5, v1
	v_or_b32_e32 v10, 8, v62
	v_mov_b32_e32 v11, v1
	v_or_b32_e32 v12, 12, v62
	v_mov_b32_e32 v13, v1
	v_or_b32_e32 v18, 16, v62
	v_mov_b32_e32 v19, v1
	v_or_b32_e32 v20, 20, v62
	v_mov_b32_e32 v21, v1
	v_or_b32_e32 v26, 24, v62
	v_mov_b32_e32 v27, v1
	v_or_b32_e32 v28, 28, v62
	v_mov_b32_e32 v29, v1
	v_or_b32_e32 v34, 32, v62
	v_mov_b32_e32 v35, v1
	v_or_b32_e32 v36, 36, v62
	v_mov_b32_e32 v37, v1
	v_or_b32_e32 v42, 40, v62
	v_mov_b32_e32 v43, v1
	v_or_b32_e32 v44, 44, v62
	v_mov_b32_e32 v45, v1
	v_or_b32_e32 v50, 48, v62
	v_mov_b32_e32 v51, v1
	v_or_b32_e32 v52, 52, v62
	v_mov_b32_e32 v53, v1
	v_lshl_add_u64 v[64:65], s[14:15], 0, v[0:1]
	v_lshlrev_b64 v[2:3], 12, v[62:63]
	v_lshlrev_b64 v[4:5], 12, v[4:5]
	v_lshlrev_b64 v[10:11], 12, v[10:11]
	v_lshlrev_b64 v[12:13], 12, v[12:13]
	v_lshlrev_b64 v[18:19], 12, v[18:19]
	v_lshlrev_b64 v[20:21], 12, v[20:21]
	v_lshlrev_b64 v[26:27], 12, v[26:27]
	v_lshlrev_b64 v[28:29], 12, v[28:29]
	v_lshlrev_b64 v[34:35], 12, v[34:35]
	v_lshlrev_b64 v[36:37], 12, v[36:37]
	v_lshlrev_b64 v[42:43], 12, v[42:43]
	v_lshlrev_b64 v[44:45], 12, v[44:45]
	v_lshlrev_b64 v[50:51], 12, v[50:51]
	v_lshlrev_b64 v[52:53], 12, v[52:53]
	v_lshl_add_u64 v[2:3], v[64:65], 0, v[2:3]
	v_lshl_add_u64 v[6:7], v[64:65], 0, v[4:5]
	v_lshl_add_u64 v[10:11], v[64:65], 0, v[10:11]
	v_lshl_add_u64 v[14:15], v[64:65], 0, v[12:13]
	v_lshl_add_u64 v[18:19], v[64:65], 0, v[18:19]
	v_lshl_add_u64 v[22:23], v[64:65], 0, v[20:21]
	v_lshl_add_u64 v[26:27], v[64:65], 0, v[26:27]
	v_lshl_add_u64 v[30:31], v[64:65], 0, v[28:29]
	v_lshl_add_u64 v[34:35], v[64:65], 0, v[34:35]
	v_lshl_add_u64 v[38:39], v[64:65], 0, v[36:37]
	v_lshl_add_u64 v[42:43], v[64:65], 0, v[42:43]
	v_lshl_add_u64 v[46:47], v[64:65], 0, v[44:45]
	v_lshl_add_u64 v[50:51], v[64:65], 0, v[50:51]
	v_lshl_add_u64 v[54:55], v[64:65], 0, v[52:53]
	global_load_dwordx4 v[2:5], v[2:3], off nt
	s_nop 0
	global_load_dwordx4 v[6:9], v[6:7], off nt
	s_nop 0
	global_load_dwordx4 v[10:13], v[10:11], off nt
	s_nop 0
	global_load_dwordx4 v[14:17], v[14:15], off nt
	s_nop 0
	global_load_dwordx4 v[18:21], v[18:19], off nt
	s_nop 0
	global_load_dwordx4 v[22:25], v[22:23], off nt
	s_nop 0
	global_load_dwordx4 v[26:29], v[26:27], off nt
	s_nop 0
	global_load_dwordx4 v[30:33], v[30:31], off nt
	s_nop 0
	global_load_dwordx4 v[34:37], v[34:35], off nt
	s_nop 0
	global_load_dwordx4 v[38:41], v[38:39], off nt
	s_nop 0
	global_load_dwordx4 v[42:45], v[42:43], off nt
	s_nop 0
	global_load_dwordx4 v[46:49], v[46:47], off nt
	s_nop 0
	global_load_dwordx4 v[50:53], v[50:51], off nt
	s_nop 0
	global_load_dwordx4 v[54:57], v[54:55], off nt
	v_or_b32_e32 v58, 56, v62
	v_mov_b32_e32 v59, v1
	v_lshlrev_b64 v[58:59], 12, v[58:59]
	v_lshl_add_u64 v[58:59], v[64:65], 0, v[58:59]
	v_or_b32_e32 v62, 60, v62
	global_load_dwordx4 v[58:61], v[58:59], off nt
	v_lshlrev_b64 v[62:63], 12, v[62:63]
	v_lshl_add_u64 v[62:63], v[64:65], 0, v[62:63]
	global_load_dwordx4 v[62:65], v[62:63], off nt
	s_lshl_b64 s[14:15], s[88:89], 1
	s_add_u32 s14, s9, s14
	s_addc_u32 s15, s30, s15
	v_mov_b32_e32 v103, v1
	s_waitcnt vmcnt(0)
; #define LAS __attribute__((address_space(3)))
; __device__ __forceinline__ unsigned pk2(float lo, float hi) { f32x2_cv_ v = {lo, hi}; return __builtin_bit_cast(unsigned, __builtin_convertvector(v, bf16x2_cv_)); }
; __device__ __forceinline__ void prep_item64(const float* W, int ldw, int srccol0, const float* g, bf16_t* dstrow0, int K, int k0, LAS float* scr, int lane) {
;     ...
;     for (int i = 0; i < 16; ++i) { const float gg = g ? g[k0 + 4 * i + kq] : 1.f; LAS float* d = scr + (4 * i + kq) * 65 + n4; d[0] = v[i][0] * gg; d[1] = v[i][1] * gg; d[2] = v[i][2] * gg; d[3] = v[i][3] * gg; }
;     asm volatile("s_waitcnt lgkmcnt(0)" ::: "memory");
;     const int c = lane & 7;
; #pragma unroll
;     for (int j = 0; j < 8; ++j) { const int n = (lane >> 3) + 8 * j; const LAS float* s = scr + (8 * c) * 65 + n;
;         u32x4 o; o.x = pk2(s[0 * 65], s[1 * 65]); o.y = pk2(s[2 * 65], s[3 * 65]); o.z = pk2(s[4 * 65], s[5 * 65]); o.w = pk2(s[6 * 65], s[7 * 65]);
;         *(u32x4*)(dstrow0 + (size_t)n * K + k0 + 8 * c) = o; }
;     asm volatile("s_waitcnt lgkmcnt(0)" ::: "memory");
	ds_write2_b32 v106, v2, v3 offset1:1
	ds_write2_b32 v106, v4, v5 offset0:2 offset1:3
	ds_write2_b32 v108, v6, v7 offset1:1
	ds_write2_b32 v109, v8, v9 offset1:1
	ds_write2_b32 v110, v10, v11 offset1:1
	ds_write2_b32 v137, v12, v13 offset1:1
	ds_write2_b32 v136, v14, v15 offset1:1
	ds_write2_b32 v135, v16, v17 offset1:1
	ds_write2_b32 v133, v18, v19 offset1:1
	ds_write2_b32 v134, v20, v21 offset1:1
	ds_write2_b32 v132, v22, v23 offset1:1
	ds_write2_b32 v131, v24, v25 offset1:1
	ds_write2_b32 v129, v26, v27 offset1:1
	ds_write2_b32 v130, v28, v29 offset1:1
	ds_write2_b32 v128, v30, v31 offset1:1
	ds_write2_b32 v127, v32, v33 offset1:1
	ds_write2_b32 v125, v34, v35 offset1:1
	ds_write2_b32 v126, v36, v37 offset1:1
	ds_write2_b32 v124, v38, v39 offset1:1
	ds_write2_b32 v123, v40, v41 offset1:1
	ds_write2_b32 v121, v42, v43 offset1:1
	ds_write2_b32 v122, v44, v45 offset1:1
	ds_write2_b32 v120, v46, v47 offset1:1
	ds_write2_b32 v119, v48, v49 offset1:1
	ds_write2_b32 v117, v50, v51 offset1:1
	ds_write2_b32 v118, v52, v53 offset1:1
	ds_write2_b32 v116, v54, v55 offset1:1
	ds_write2_b32 v115, v56, v57 offset1:1
	ds_write2_b32 v113, v58, v59 offset1:1
	ds_write2_b32 v114, v60, v61 offset1:1
	ds_write2_b32 v112, v62, v63 offset1:1
	ds_write2_b32 v111, v64, v65 offset1:1
	s_waitcnt lgkmcnt(0)
	ds_read_b32 v2, v107
	ds_read_b32 v3, v107 offset:260
	ds_read_b32 v4, v107 offset:520
	ds_read_b32 v5, v107 offset:780
	ds_read_b32 v8, v107 offset:1040
	ds_read_b32 v9, v107 offset:1300
	ds_read_b32 v10, v107 offset:1560
	ds_read_b32 v11, v107 offset:1820
	v_lshl_add_u64 v[6:7], s[14:15], 0, v[102:103]
	s_waitcnt lgkmcnt(0)
	v_cvt_pk_bf16_f32 v2, v2, v3
	s_waitcnt lgkmcnt(4)
	v_cvt_pk_bf16_f32 v3, v4, v5
	s_waitcnt lgkmcnt(2)
	v_cvt_pk_bf16_f32 v4, v8, v9
	s_waitcnt lgkmcnt(0)
	v_cvt_pk_bf16_f32 v5, v10, v11
	v_lshl_add_u64 v[8:9], v[6:7], 0, v[70:71]
	flat_store_dwordx4 v[8:9], v[2:5] nt
	ds_read_b32 v2, v107 offset:32
	ds_read_b32 v3, v107 offset:292
	ds_read_b32 v4, v107 offset:552
	ds_read_b32 v5, v107 offset:812
	ds_read_b32 v8, v107 offset:1072
	ds_read_b32 v9, v107 offset:1332
	ds_read_b32 v10, v107 offset:1592
	ds_read_b32 v11, v107 offset:1852
	s_waitcnt lgkmcnt(0)
	v_cvt_pk_bf16_f32 v2, v2, v3
	v_cvt_pk_bf16_f32 v3, v4, v5
	v_cvt_pk_bf16_f32 v4, v8, v9
	v_lshl_add_u64 v[8:9], v[6:7], 0, v[72:73]
	v_cvt_pk_bf16_f32 v5, v10, v11
	flat_store_dwordx4 v[8:9], v[2:5] nt
	ds_read_b32 v2, v107 offset:64
	ds_read_b32 v3, v107 offset:324
	ds_read_b32 v4, v107 offset:584
	ds_read_b32 v5, v107 offset:844
	ds_read_b32 v8, v107 offset:1104
	ds_read_b32 v9, v107 offset:1364
	ds_read_b32 v10, v107 offset:1624
	ds_read_b32 v11, v107 offset:1884
	s_waitcnt lgkmcnt(0)
	v_cvt_pk_bf16_f32 v2, v2, v3
	v_cvt_pk_bf16_f32 v3, v4, v5
	v_cvt_pk_bf16_f32 v4, v8, v9
	v_lshl_add_u64 v[8:9], v[6:7], 0, v[74:75]
	v_cvt_pk_bf16_f32 v5, v10, v11
	flat_store_dwordx4 v[8:9], v[2:5] nt
	ds_read_b32 v2, v107 offset:96
	ds_read_b32 v3, v107 offset:356
	ds_read_b32 v4, v107 offset:616
	ds_read_b32 v5, v107 offset:876
	ds_read_b32 v8, v107 offset:1136
	ds_read_b32 v9, v107 offset:1396
	ds_read_b32 v10, v107 offset:1656
	ds_read_b32 v11, v107 offset:1916
	s_waitcnt lgkmcnt(0)
	v_cvt_pk_bf16_f32 v2, v2, v3
	v_cvt_pk_bf16_f32 v3, v4, v5
	v_cvt_pk_bf16_f32 v4, v8, v9
	v_lshl_add_u64 v[8:9], v[6:7], 0, v[76:77]
	v_cvt_pk_bf16_f32 v5, v10, v11
	flat_store_dwordx4 v[8:9], v[2:5] nt
	ds_read_b32 v2, v107 offset:128
	ds_read_b32 v3, v107 offset:388
	ds_read_b32 v4, v107 offset:648
	ds_read_b32 v5, v107 offset:908
	ds_read_b32 v8, v107 offset:1168
	ds_read_b32 v9, v107 offset:1428
	ds_read_b32 v10, v107 offset:1688
	ds_read_b32 v11, v107 offset:1948
	s_waitcnt lgkmcnt(0)
	v_cvt_pk_bf16_f32 v2, v2, v3
	v_cvt_pk_bf16_f32 v3, v4, v5
	v_cvt_pk_bf16_f32 v4, v8, v9
	v_lshl_add_u64 v[8:9], v[6:7], 0, v[78:79]
	v_cvt_pk_bf16_f32 v5, v10, v11
	flat_store_dwordx4 v[8:9], v[2:5] nt
	ds_read_b32 v2, v107 offset:160
	ds_read_b32 v3, v107 offset:420
	ds_read_b32 v4, v107 offset:680
	ds_read_b32 v5, v107 offset:940
	ds_read_b32 v8, v107 offset:1200
	ds_read_b32 v9, v107 offset:1460
	ds_read_b32 v10, v107 offset:1720
	ds_read_b32 v11, v107 offset:1980
	s_waitcnt lgkmcnt(0)
	v_cvt_pk_bf16_f32 v2, v2, v3
	v_cvt_pk_bf16_f32 v3, v4, v5
	v_cvt_pk_bf16_f32 v4, v8, v9
	v_lshl_add_u64 v[8:9], v[6:7], 0, v[80:81]
	v_cvt_pk_bf16_f32 v5, v10, v11
	flat_store_dwordx4 v[8:9], v[2:5] nt
	ds_read_b32 v2, v107 offset:192
	ds_read_b32 v3, v107 offset:452
	ds_read_b32 v4, v107 offset:712
	ds_read_b32 v5, v107 offset:972
	ds_read_b32 v8, v107 offset:1232
	ds_read_b32 v9, v107 offset:1492
	ds_read_b32 v10, v107 offset:1752
	ds_read_b32 v11, v107 offset:2012
	s_waitcnt lgkmcnt(0)
	v_cvt_pk_bf16_f32 v2, v2, v3
	v_cvt_pk_bf16_f32 v3, v4, v5
	v_cvt_pk_bf16_f32 v4, v8, v9
	v_lshl_add_u64 v[8:9], v[6:7], 0, v[82:83]
	v_cvt_pk_bf16_f32 v5, v10, v11
	flat_store_dwordx4 v[8:9], v[2:5] nt
	ds_read_b32 v2, v107 offset:224
	ds_read_b32 v3, v107 offset:484
	ds_read_b32 v4, v107 offset:744
	ds_read_b32 v5, v107 offset:1004
	ds_read_b32 v8, v107 offset:1264
	ds_read_b32 v9, v107 offset:1524
	ds_read_b32 v10, v107 offset:1784
	ds_read_b32 v11, v107 offset:2044
	s_waitcnt lgkmcnt(0)
	v_cvt_pk_bf16_f32 v2, v2, v3
	v_cvt_pk_bf16_f32 v3, v4, v5
	v_cvt_pk_bf16_f32 v4, v8, v9
	v_lshl_add_u64 v[6:7], v[6:7], 0, v[84:85]
	v_cvt_pk_bf16_f32 v5, v10, v11
	flat_store_dwordx4 v[6:7], v[2:5] nt
	s_waitcnt lgkmcnt(0)
	s_mov_b64 s[14:15], 0
